# P0 x row loads: system-scope nt (sc0 sc1 nt) instead of nt
# baseline (speedup 1.0000x reference)
; __device__ __forceinline__ void rms_row_i8(const float* xrow, const float* gain, unsigned char* qrow, float* qscale, int lane) {
;     const f32x4* xr = (const f32x4*)xrow + lane; const f32x4* gr = (const f32x4*)gain + lane;
;     f32x4 v[16]; float s = 0.f;
; #pragma unroll
;     for (int j = 0; j < 16; ++j) { v[j] = xr[64 * j]; s += (v[j].x * v[j].x + v[j].y * v[j].y) + (v[j].z * v[j].z + v[j].w * v[j].w); }
;     const float rstd = 1.f / sqrtf(wave_sum(s) * (1.f / D) + RMS_EPS);
; __device__ __forceinline__ void phase_prologue(const Frame& F, const Args& a) {
;     ...
;           for (int j = 0; j < 4; ++j) { const int m = m0 + 4 * F.wave + j; rms_row_i8(a.in[0] + (size_t)m * D, a.in[2], ws + WS_A + (size_t)m * D, (float*)(ws + SA_H) + m, F.lane); } } }
.LBB0_93:
	v_lshl_add_u64 v[46:47], v[98:99], 0, s[14:15]
	global_load_dwordx4 v[38:41], v[46:47], off sc0 sc1 nt
	global_load_dwordx4 v[30:33], v[46:47], off offset:1024 sc0 sc1 nt
	global_load_dwordx4 v[2:5], v[46:47], off offset:3072 sc0 sc1 nt
	global_load_dwordx4 v[18:21], v[46:47], off offset:2048 sc0 sc1 nt
	v_add_co_u32_e32 v116, vcc, s21, v46
	s_waitcnt vmcnt(2)
	v_pk_mul_f32 v[120:121], v[32:33], v[32:33]
	v_addc_co_u32_e32 v117, vcc, 0, v47, vcc
	global_load_dwordx4 v[6:9], v[116:117], off offset:-4096 sc0 sc1 nt
	v_add_co_u32_e32 v48, vcc, s20, v46
	v_pk_mul_f32 v[122:123], v[30:31], v[30:31]
	s_nop 0
	v_addc_co_u32_e32 v49, vcc, 0, v47, vcc
	global_load_dwordx4 v[10:13], v[48:49], off offset:2048 sc0 sc1 nt
	global_load_dwordx4 v[14:17], v[48:49], off offset:1024 sc0 sc1 nt
	global_load_dwordx4 v[26:29], v[48:49], off offset:3072 sc0 sc1 nt
	global_load_dwordx4 v[22:25], v[116:117], off offset:1024 sc0 sc1 nt
	global_load_dwordx4 v[34:37], v[116:117], off sc0 sc1 nt
	global_load_dwordx4 v[42:45], v[116:117], off offset:2048 sc0 sc1 nt
	v_add_co_u32_e32 v118, vcc, s22, v46
	s_waitcnt vmcnt(7)
	v_mul_f32_e32 v124, v19, v19
	v_addc_co_u32_e32 v119, vcc, 0, v47, vcc
	global_load_dwordx4 v[50:53], v[116:117], off offset:3072 sc0 sc1 nt
	global_load_dwordx4 v[46:49], v[118:119], off sc0 sc1 nt
	global_load_dwordx4 v[58:61], v[118:119], off offset:1024 sc0 sc1 nt
	global_load_dwordx4 v[62:65], v[118:119], off offset:2048 sc0 sc1 nt
	global_load_dwordx4 v[54:57], v[118:119], off offset:3072 sc0 sc1 nt
	v_pk_mul_f32 v[116:117], v[40:41], v[40:41]
	v_pk_mul_f32 v[118:119], v[38:39], v[38:39]
	v_mul_f32_e32 v126, v21, v21
	v_pk_mov_b32 v[128:129], v[118:119], v[116:117] op_sel:[1,0]
	v_mov_b32_e32 v119, v117
	v_pk_mov_b32 v[116:117], v[122:123], v[120:121] op_sel:[1,0]
	v_mov_b32_e32 v123, v121
	v_pk_add_f32 v[118:119], v[128:129], v[118:119]
	v_pk_add_f32 v[116:117], v[116:117], v[122:123]
	v_mul_f32_e32 v141, v2, v2
	v_mul_f32_e32 v142, v3, v3
	v_mul_f32_e32 v133, v4, v4
	v_mul_f32_e32 v135, v5, v5
	v_pk_fma_f32 v[120:121], v[18:19], v[18:19], v[124:125] op_sel_hi:[1,1,0]
	v_pk_fma_f32 v[124:125], v[20:21], v[20:21], v[126:127] op_sel_hi:[1,1,0]
	v_pk_add_f32 v[118:119], v[118:119], v[118:119] op_sel:[0,1] op_sel_hi:[1,0]
	v_pk_add_f32 v[116:117], v[116:117], v[116:117] op_sel:[0,1] op_sel_hi:[1,0]
	v_mov_b32_e32 v121, v133
	v_mov_b32_e32 v125, v135
	v_mov_b32_e32 v119, v141
	v_mov_b32_e32 v117, v142
	v_pk_add_f32 v[120:121], v[120:121], v[124:125]
	v_pk_add_f32 v[116:117], v[118:119], v[116:117]
	s_waitcnt vmcnt(11)
	v_pk_mul_f32 v[126:127], v[8:9], v[8:9]
	v_pk_mul_f32 v[130:131], v[6:7], v[6:7]
	s_waitcnt vmcnt(9)
	v_mul_f32_e32 v132, v15, v15
	v_pk_mov_b32 v[122:123], v[130:131], v[126:127] op_sel:[1,0]
	v_mov_b32_e32 v131, v127
	v_mul_f32_e32 v134, v17, v17
	v_pk_add_f32 v[122:123], v[122:123], v[130:131]
	v_pk_add_f32 v[116:117], v[116:117], v[120:121]
	v_mul_f32_e32 v143, v10, v10
	v_mul_f32_e32 v144, v11, v11
	v_mul_f32_e32 v145, v12, v12
	v_mul_f32_e32 v146, v13, v13
	v_pk_fma_f32 v[126:127], v[14:15], v[14:15], v[132:133] op_sel_hi:[1,1,0]
	v_pk_fma_f32 v[128:129], v[16:17], v[16:17], v[134:135] op_sel_hi:[1,1,0]
	v_pk_add_f32 v[122:123], v[122:123], v[122:123] op_sel:[0,1] op_sel_hi:[1,0]
	v_pk_add_f32 v[116:117], v[116:117], v[116:117] op_sel:[0,1] op_sel_hi:[1,0]
	s_waitcnt vmcnt(8)
	v_pk_mul_f32 v[136:137], v[28:29], v[28:29]
	v_pk_mul_f32 v[138:139], v[26:27], v[26:27]
	v_mov_b32_e32 v127, v145
	v_mov_b32_e32 v129, v146
	v_mov_b32_e32 v123, v144
	v_mov_b32_e32 v117, v143
	v_pk_mov_b32 v[132:133], v[138:139], v[136:137] op_sel:[1,0]
	v_mov_b32_e32 v139, v137
	v_pk_add_f32 v[126:127], v[126:127], v[128:129]
	v_pk_add_f32 v[116:117], v[116:117], v[122:123]
	s_waitcnt vmcnt(6)
	v_mul_f32_e32 v140, v35, v35
	v_pk_add_f32 v[124:125], v[132:133], v[138:139]
	v_pk_add_f32 v[116:117], v[116:117], v[126:127]
	v_mul_f32_e32 v118, v37, v37
	v_mul_f32_e32 v147, v22, v22
	v_mul_f32_e32 v148, v23, v23
	v_mul_f32_e32 v149, v24, v24
	v_mul_f32_e32 v150, v25, v25
	v_pk_fma_f32 v[134:135], v[34:35], v[34:35], v[140:141] op_sel_hi:[1,1,0]
	v_pk_add_f32 v[124:125], v[124:125], v[124:125] op_sel:[0,1] op_sel_hi:[1,0]
	v_pk_add_f32 v[116:117], v[116:117], v[116:117] op_sel:[0,1] op_sel_hi:[1,0]
	v_pk_fma_f32 v[118:119], v[36:37], v[36:37], v[118:119] op_sel_hi:[1,1,0]
	v_mov_b32_e32 v135, v149
	v_mov_b32_e32 v125, v148
	v_mov_b32_e32 v117, v147
	v_mov_b32_e32 v119, v150
	v_pk_add_f32 v[116:117], v[116:117], v[124:125]
	v_pk_add_f32 v[118:119], v[134:135], v[118:119]
	s_waitcnt vmcnt(5)
	v_pk_mul_f32 v[120:121], v[42:43], v[42:43]
	v_pk_add_f32 v[116:117], v[116:117], v[118:119]
	v_pk_mul_f32 v[118:119], v[44:45], v[44:45]
	v_pk_add_f32 v[116:117], v[116:117], v[116:117] op_sel:[0,1] op_sel_hi:[1,0]
	v_pk_mov_b32 v[122:123], v[120:121], v[118:119] op_sel:[1,0]
	v_mov_b32_e32 v121, v119
	v_pk_add_f32 v[118:119], v[122:123], v[120:121]
	s_waitcnt vmcnt(3)
	v_mul_f32_e32 v120, v46, v46
	v_mul_f32_e32 v121, v47, v47
	v_pk_add_f32 v[118:119], v[118:119], v[118:119] op_sel:[0,1] op_sel_hi:[1,0]
	v_mov_b32_e32 v117, v120
	v_mov_b32_e32 v119, v121
	v_pk_add_f32 v[116:117], v[116:117], v[118:119]
	v_mul_f32_e32 v118, v51, v51
	v_mul_f32_e32 v120, v53, v53
	v_mul_f32_e32 v122, v48, v48
	v_mul_f32_e32 v123, v49, v49
	v_pk_fma_f32 v[118:119], v[50:51], v[50:51], v[118:119] op_sel_hi:[1,1,0]
	v_pk_fma_f32 v[120:121], v[52:53], v[52:53], v[120:121] op_sel_hi:[1,1,0]
	v_mov_b32_e32 v119, v122
	v_mov_b32_e32 v121, v123
	v_pk_add_f32 v[118:119], v[118:119], v[120:121]
	s_waitcnt vmcnt(2)
; __device__ __forceinline__ void rms_row_i8(const float* xrow, const float* gain, unsigned char* qrow, float* qscale, int lane) {
;     ...
;     for (int j = 0; j < 16; ++j) { v[j] = xr[64 * j]; s += (v[j].x * v[j].x + v[j].y * v[j].y) + (v[j].z * v[j].z + v[j].w * v[j].w); }
;     const float rstd = 1.f / sqrtf(wave_sum(s) * (1.f / D) + RMS_EPS);
;     float amax = 0.f;
; #pragma unroll
;     for (int j = 0; j < 16; ++j) { v[j] = v[j] * rstd * gr[64 * j]; amax = fmaxf(fmaxf(amax, fmaxf(fabsf(v[j].x), fabsf(v[j].y))), fmaxf(fabsf(v[j].z), fabsf(v[j].w))); }
	v_pk_mul_f32 v[120:121], v[58:59], v[58:59]
	v_pk_add_f32 v[116:117], v[116:117], v[118:119]
	v_pk_mul_f32 v[118:119], v[60:61], v[60:61]
	v_pk_add_f32 v[116:117], v[116:117], v[116:117] op_sel:[0,1] op_sel_hi:[1,0]
	v_pk_mov_b32 v[122:123], v[120:121], v[118:119] op_sel:[1,0]
	v_mov_b32_e32 v121, v119
	v_pk_add_f32 v[118:119], v[122:123], v[120:121]
	s_waitcnt vmcnt(0)
	v_mul_f32_e32 v120, v54, v54
	v_mul_f32_e32 v121, v55, v55
	v_pk_add_f32 v[118:119], v[118:119], v[118:119] op_sel:[0,1] op_sel_hi:[1,0]
	v_mov_b32_e32 v117, v120
	v_mov_b32_e32 v119, v121
	v_pk_add_f32 v[116:117], v[116:117], v[118:119]
	v_mul_f32_e32 v118, v63, v63
	v_mul_f32_e32 v120, v65, v65
	v_mul_f32_e32 v122, v56, v56
	v_mul_f32_e32 v123, v57, v57
	v_pk_fma_f32 v[118:119], v[62:63], v[62:63], v[118:119] op_sel_hi:[1,1,0]
	v_pk_fma_f32 v[120:121], v[64:65], v[64:65], v[120:121] op_sel_hi:[1,1,0]
	v_mov_b32_e32 v119, v122
	v_mov_b32_e32 v121, v123
	v_pk_add_f32 v[118:119], v[118:119], v[120:121]
	global_load_dwordx4 v[140:143], v[76:77], off
	v_pk_add_f32 v[116:117], v[116:117], v[118:119]
	s_nop 0
	v_add_f32_e32 v120, v116, v117
	ds_bpermute_b32 v121, v110, v120
	global_load_dwordx4 v[116:119], v[70:71], off
	s_waitcnt lgkmcnt(0)
	v_add_f32_e32 v124, v120, v121
	ds_bpermute_b32 v125, v111, v124
	global_load_dwordx4 v[120:123], v[70:71], off offset:1024
	s_waitcnt lgkmcnt(0)
	v_add_f32_e32 v124, v124, v125
	ds_bpermute_b32 v125, v112, v124
	s_waitcnt lgkmcnt(0)
	v_add_f32_e32 v128, v124, v125
	global_load_dwordx4 v[124:127], v[70:71], off offset:2048
	ds_bpermute_b32 v129, v113, v128
	s_waitcnt lgkmcnt(0)
	v_add_f32_e32 v132, v128, v129
	ds_bpermute_b32 v133, v114, v132
	global_load_dwordx4 v[128:131], v[70:71], off offset:3072
	s_waitcnt lgkmcnt(0)
	v_add_f32_e32 v136, v132, v133
	ds_bpermute_b32 v137, v115, v136
	global_load_dwordx4 v[132:135], v[72:73], off
	s_waitcnt lgkmcnt(0)
	v_add_f32_e32 v136, v136, v137
	v_fmamk_f32 v136, v136, 0x39800000, v108
	v_mul_f32_e32 v137, 0x4f800000, v136
	v_cmp_gt_f32_e32 vcc, s23, v136
	s_nop 1
	v_cndmask_b32_e32 v148, v136, v137, vcc
	v_sqrt_f32_e32 v144, v148
	global_load_dwordx4 v[136:139], v[74:75], off
	v_add_u32_e32 v145, -1, v144
	v_fma_f32 v146, -v145, v144, v148
	v_cmp_ge_f32_e64 s[8:9], 0, v146
	v_add_u32_e32 v146, 1, v144
	s_nop 0
	v_cndmask_b32_e64 v145, v144, v145, s[8:9]
	v_fma_f32 v144, -v146, v144, v148
	v_cmp_lt_f32_e64 s[8:9], 0, v144
	s_nop 1
	v_cndmask_b32_e64 v149, v145, v146, s[8:9]
	v_mul_f32_e32 v150, 0x37800000, v149
	v_cndmask_b32_e32 v149, v149, v150, vcc
	v_cmp_class_f32_e32 vcc, v148, v109
	global_load_dwordx4 v[144:147], v[78:79], off
	s_nop 0
	v_cndmask_b32_e32 v160, v149, v148, vcc
	v_div_scale_f32 v156, s[8:9], v160, v160, 1.0
	v_rcp_f32_e32 v161, v156
	global_load_dwordx4 v[148:151], v[80:81], off
	v_div_scale_f32 v157, vcc, 1.0, v160, 1.0
	v_fma_f32 v152, -v156, v161, 1.0
	v_fmac_f32_e32 v161, v152, v161
	v_mul_f32_e32 v162, v157, v161
	global_load_dwordx4 v[152:155], v[82:83], off
	v_fma_f32 v158, -v156, v162, v157
	v_fmac_f32_e32 v162, v158, v161
	v_fma_f32 v163, -v156, v162, v157
	global_load_dwordx4 v[156:159], v[84:85], off
	v_div_fmas_f32 v161, v163, v161, v162
	v_div_fixup_f32 v160, v161, v160, 1.0
	v_pk_mul_f32 v[38:39], v[38:39], v[160:161] op_sel_hi:[1,0]
	v_pk_mul_f32 v[40:41], v[40:41], v[160:161] op_sel_hi:[1,0]
	s_waitcnt vmcnt(9)
	v_pk_mul_f32 v[164:165], v[116:117], v[38:39]
	v_pk_mul_f32 v[162:163], v[118:119], v[40:41]
	global_load_dwordx4 v[38:41], v[86:87], off
	v_max_f32_e64 v116, |v164|, |v165|
	v_max_f32_e64 v117, |v162|, |v163|
	v_max3_f32 v118, v116, 0, v117
	v_pk_mul_f32 v[116:117], v[30:31], v[160:161] op_sel_hi:[1,0]
	v_pk_mul_f32 v[30:31], v[32:33], v[160:161] op_sel_hi:[1,0]
	s_waitcnt vmcnt(9)
	v_pk_mul_f32 v[168:169], v[120:121], v[116:117]
	v_pk_mul_f32 v[166:167], v[122:123], v[30:31]
	global_load_dwordx4 v[30:33], v[88:89], off
	v_max_f32_e64 v116, |v168|, |v169|
	v_max_f32_e64 v117, |v166|, |v167|
	v_max3_f32 v120, v118, v116, v117
	v_pk_mul_f32 v[18:19], v[18:19], v[160:161] op_sel_hi:[1,0]
	v_pk_mul_f32 v[20:21], v[20:21], v[160:161] op_sel_hi:[1,0]
	global_load_dwordx4 v[116:119], v[90:91], off
	s_waitcnt vmcnt(10)
	v_pk_mul_f32 v[170:171], v[126:127], v[20:21]
	v_pk_mul_f32 v[172:173], v[124:125], v[18:19]
	v_max_f32_e64 v19, |v170|, |v171|
	v_max_f32_e64 v18, |v172|, |v173|
	v_max3_f32 v18, v120, v18, v19
	global_load_dwordx4 v[120:123], v[92:93], off
	global_load_dwordx4 v[124:127], v[94:95], off
	v_pk_mul_f32 v[2:3], v[2:3], v[160:161] op_sel_hi:[1,0]
	v_pk_mul_f32 v[4:5], v[4:5], v[160:161] op_sel_hi:[1,0]
	s_waitcnt vmcnt(11)
	v_pk_mul_f32 v[128:129], v[128:129], v[2:3]
	v_pk_mul_f32 v[130:131], v[130:131], v[4:5]
	v_max_f32_e64 v2, |v128|, |v129|
	v_max_f32_e64 v3, |v130|, |v131|
	v_max3_f32 v18, v18, v2, v3
	v_pk_mul_f32 v[2:3], v[6:7], v[160:161] op_sel_hi:[1,0]
	v_pk_mul_f32 v[4:5], v[8:9], v[160:161] op_sel_hi:[1,0]
	s_waitcnt vmcnt(10)
	v_pk_mul_f32 v[132:133], v[132:133], v[2:3]
	v_pk_mul_f32 v[134:135], v[134:135], v[4:5]
	v_max_f32_e64 v2, |v132|, |v133|
	v_max_f32_e64 v3, |v134|, |v135|
	v_max3_f32 v6, v18, v2, v3
	v_pk_mul_f32 v[2:3], v[14:15], v[160:161] op_sel_hi:[1,0]
	v_pk_mul_f32 v[4:5], v[16:17], v[160:161] op_sel_hi:[1,0]
	s_waitcnt vmcnt(9)
	v_pk_mul_f32 v[136:137], v[136:137], v[2:3]
	v_pk_mul_f32 v[138:139], v[138:139], v[4:5]
	v_max_f32_e64 v2, |v136|, |v137|
	v_max_f32_e64 v3, |v138|, |v139|
	v_max3_f32 v6, v6, v2, v3
	v_pk_mul_f32 v[2:3], v[10:11], v[160:161] op_sel_hi:[1,0]
	v_pk_mul_f32 v[4:5], v[12:13], v[160:161] op_sel_hi:[1,0]
	v_pk_mul_f32 v[140:141], v[140:141], v[2:3]
	v_pk_mul_f32 v[142:143], v[142:143], v[4:5]
	v_max_f32_e64 v2, |v140|, |v141|
	v_max_f32_e64 v3, |v142|, |v143|
	v_max3_f32 v6, v6, v2, v3
	v_pk_mul_f32 v[2:3], v[26:27], v[160:161] op_sel_hi:[1,0]
	v_pk_mul_f32 v[4:5], v[28:29], v[160:161] op_sel_hi:[1,0]
	s_waitcnt vmcnt(8)
	v_pk_mul_f32 v[144:145], v[144:145], v[2:3]
	v_pk_mul_f32 v[146:147], v[146:147], v[4:5]
	v_max_f32_e64 v2, |v144|, |v145|
	v_max_f32_e64 v3, |v146|, |v147|
	v_max3_f32 v6, v6, v2, v3
	v_pk_mul_f32 v[2:3], v[34:35], v[160:161] op_sel_hi:[1,0]
	v_pk_mul_f32 v[4:5], v[36:37], v[160:161] op_sel_hi:[1,0]
	s_waitcnt vmcnt(7)
	v_pk_mul_f32 v[36:37], v[148:149], v[2:3]
	v_pk_mul_f32 v[34:35], v[150:151], v[4:5]
	v_max_f32_e64 v2, |v36|, |v37|
	v_max_f32_e64 v3, |v34|, |v35|
	v_max3_f32 v6, v6, v2, v3
	v_pk_mul_f32 v[2:3], v[22:23], v[160:161] op_sel_hi:[1,0]
	v_pk_mul_f32 v[4:5], v[24:25], v[160:161] op_sel_hi:[1,0]
	s_waitcnt vmcnt(6)
	v_pk_mul_f32 v[150:151], v[152:153], v[2:3]
	v_pk_mul_f32 v[148:149], v[154:155], v[4:5]
	v_max_f32_e64 v2, |v150|, |v151|
	v_max_f32_e64 v3, |v148|, |v149|
	v_max3_f32 v6, v6, v2, v3
	v_pk_mul_f32 v[2:3], v[42:43], v[160:161] op_sel_hi:[1,0]
	v_pk_mul_f32 v[4:5], v[44:45], v[160:161] op_sel_hi:[1,0]
	s_waitcnt vmcnt(5)
	v_pk_mul_f32 v[26:27], v[156:157], v[2:3]
	v_pk_mul_f32 v[24:25], v[158:159], v[4:5]
	v_max_f32_e64 v2, |v26|, |v27|
	v_max_f32_e64 v3, |v24|, |v25|
	v_max3_f32 v6, v6, v2, v3
	v_pk_mul_f32 v[2:3], v[50:51], v[160:161] op_sel_hi:[1,0]
	v_pk_mul_f32 v[4:5], v[52:53], v[160:161] op_sel_hi:[1,0]
	s_waitcnt vmcnt(4)
	v_pk_mul_f32 v[22:23], v[2:3], v[38:39]
	v_pk_mul_f32 v[18:19], v[4:5], v[40:41]
	v_max_f32_e64 v2, |v22|, |v23|
	v_max_f32_e64 v3, |v18|, |v19|
	v_max3_f32 v6, v6, v2, v3
	v_pk_mul_f32 v[2:3], v[46:47], v[160:161] op_sel_hi:[1,0]
	v_pk_mul_f32 v[4:5], v[48:49], v[160:161] op_sel_hi:[1,0]
	s_waitcnt vmcnt(3)
	v_pk_mul_f32 v[16:17], v[2:3], v[30:31]
	v_pk_mul_f32 v[14:15], v[4:5], v[32:33]
	v_max_f32_e64 v2, |v16|, |v17|
	v_max_f32_e64 v3, |v14|, |v15|
	v_max3_f32 v6, v6, v2, v3
	v_pk_mul_f32 v[2:3], v[58:59], v[160:161] op_sel_hi:[1,0]
	v_pk_mul_f32 v[4:5], v[60:61], v[160:161] op_sel_hi:[1,0]
	s_waitcnt vmcnt(2)
	v_pk_mul_f32 v[12:13], v[2:3], v[116:117]
	v_pk_mul_f32 v[10:11], v[4:5], v[118:119]
	v_max_f32_e64 v2, |v12|, |v13|
	v_max_f32_e64 v3, |v10|, |v11|
	v_max3_f32 v20, v6, v2, v3
	v_pk_mul_f32 v[2:3], v[62:63], v[160:161] op_sel_hi:[1,0]
	v_pk_mul_f32 v[4:5], v[64:65], v[160:161] op_sel_hi:[1,0]
	s_waitcnt vmcnt(1)
	v_pk_mul_f32 v[8:9], v[2:3], v[120:121]
	v_pk_mul_f32 v[6:7], v[4:5], v[122:123]
	v_max_f32_e64 v2, |v8|, |v9|
	v_max_f32_e64 v3, |v6|, |v7|
	v_max3_f32 v20, v20, v2, v3
	v_pk_mul_f32 v[4:5], v[54:55], v[160:161] op_sel_hi:[1,0]
	v_pk_mul_f32 v[2:3], v[56:57], v[160:161] op_sel_hi:[1,0]
	s_waitcnt vmcnt(0)
	v_pk_mul_f32 v[4:5], v[4:5], v[124:125]
	v_pk_mul_f32 v[2:3], v[2:3], v[126:127]
	v_max_f32_e64 v21, |v4|, |v5|
	v_max_f32_e64 v28, |v2|, |v3|
	v_max3_f32 v20, v20, v21, v28
	ds_bpermute_b32 v21, v110, v20
	s_waitcnt lgkmcnt(0)
	v_max_f32_e32 v21, v21, v21
	v_max_f32_e32 v20, v20, v21
	ds_bpermute_b32 v21, v111, v20
	s_waitcnt lgkmcnt(0)
	v_max_f32_e32 v21, v21, v21
	v_max_f32_e32 v20, v20, v21
	ds_bpermute_b32 v21, v112, v20
	s_waitcnt lgkmcnt(0)
	v_max_f32_e32 v21, v21, v21
	v_max_f32_e32 v20, v20, v21
	ds_bpermute_b32 v21, v113, v20
	s_waitcnt lgkmcnt(0)
	v_max_f32_e32 v21, v21, v21
	v_max_f32_e32 v20, v20, v21
	ds_bpermute_b32 v21, v114, v20
	s_waitcnt lgkmcnt(0)
	v_max_f32_e32 v21, v21, v21
	v_max_f32_e32 v20, v20, v21
	ds_bpermute_b32 v21, v115, v20
	s_waitcnt lgkmcnt(0)
	v_max_f32_e32 v21, v21, v21
	v_max_f32_e32 v28, v20, v21
	v_div_scale_f32 v20, s[8:9], v28, v28, s24
	v_rcp_f32_e32 v21, v20
	s_nop 0
	v_fma_f32 v29, -v20, v21, 1.0
	v_fmac_f32_e32 v21, v29, v21
	v_div_scale_f32 v29, vcc, s24, v28, s24
	v_mul_f32_e32 v30, v29, v21
	v_fma_f32 v31, -v20, v30, v29
	v_fmac_f32_e32 v30, v31, v21
	v_fma_f32 v20, -v20, v30, v29
	v_div_fmas_f32 v20, v20, v21, v30
	v_div_fixup_f32 v20, v20, v28, s24
	v_cmp_lt_f32_e32 vcc, 0, v28
	s_nop 1
	v_cndmask_b32_e32 v29, 0, v20, vcc
	v_mul_f32_e32 v21, v165, v29
	v_mul_f32_e32 v20, v164, v29
	v_mul_f32_e32 v30, v162, v29
	v_mul_f32_e32 v31, v163, v29
	v_rndne_f32_e32 v21, v21
	v_rndne_f32_e32 v20, v20
	v_cvt_i32_f32_e32 v21, v21
	v_rndne_f32_e32 v30, v30
	v_rndne_f32_e32 v31, v31
	v_cvt_i32_f32_e32 v20, v20
	v_cvt_i32_f32_sdwa v30, v30 dst_sel:WORD_1 dst_unused:UNUSED_PAD src0_sel:DWORD
	v_cvt_i32_f32_e32 v31, v31
	v_lshlrev_b32_e32 v21, 8, v21
	v_and_b32_e32 v21, 0xff00, v21
	v_and_b32_e32 v30, 0xff0000, v30
	v_perm_b32 v20, v31, v20, s25
	v_or3_b32 v30, v20, v21, v30
	v_lshl_add_u64 v[20:21], s[4:5], 0, v[100:101]
	v_add_co_u32_e32 v20, vcc, s26, v20
	v_mul_f32_e32 v31, v169, v29
	s_nop 0
	v_addc_co_u32_e32 v21, vcc, 0, v21, vcc
	global_store_dword v[20:21], v30, off
	v_mul_f32_e32 v30, v168, v29
	v_mul_f32_e32 v32, v166, v29
	v_mul_f32_e32 v33, v167, v29
	v_rndne_f32_e32 v31, v31
	v_rndne_f32_e32 v30, v30
	v_cvt_i32_f32_e32 v31, v31
	v_rndne_f32_e32 v32, v32
	v_rndne_f32_e32 v33, v33
	v_cvt_i32_f32_e32 v30, v30
	v_cvt_i32_f32_sdwa v32, v32 dst_sel:WORD_1 dst_unused:UNUSED_PAD src0_sel:DWORD
	v_cvt_i32_f32_e32 v33, v33
	v_lshlrev_b32_e32 v31, 8, v31
	v_and_b32_e32 v31, 0xff00, v31
	v_and_b32_e32 v32, 0xff0000, v32
	v_perm_b32 v30, v33, v30, s25
	v_or3_b32 v30, v30, v31, v32
	v_mul_f32_e32 v31, v173, v29
	global_store_dword v[20:21], v30, off offset:256
	v_mul_f32_e32 v30, v172, v29
	v_mul_f32_e32 v32, v170, v29
	v_mul_f32_e32 v33, v171, v29
	v_rndne_f32_e32 v31, v31
	v_rndne_f32_e32 v30, v30
	v_cvt_i32_f32_e32 v31, v31
	v_rndne_f32_e32 v32, v32
	v_rndne_f32_e32 v33, v33
	v_cvt_i32_f32_e32 v30, v30
	v_cvt_i32_f32_sdwa v32, v32 dst_sel:WORD_1 dst_unused:UNUSED_PAD src0_sel:DWORD
	v_cvt_i32_f32_e32 v33, v33
	v_lshlrev_b32_e32 v31, 8, v31
	v_and_b32_e32 v31, 0xff00, v31
	v_and_b32_e32 v32, 0xff0000, v32
	v_perm_b32 v30, v33, v30, s25
	v_or3_b32 v30, v30, v31, v32
	v_mul_f32_e32 v31, v129, v29
	global_store_dword v[20:21], v30, off offset:512
	v_mul_f32_e32 v30, v128, v29
	v_mul_f32_e32 v32, v130, v29
	v_mul_f32_e32 v33, v131, v29
	v_rndne_f32_e32 v31, v31
	v_rndne_f32_e32 v30, v30
	v_cvt_i32_f32_e32 v31, v31
	v_rndne_f32_e32 v32, v32
	v_rndne_f32_e32 v33, v33
	v_cvt_i32_f32_e32 v30, v30
	v_cvt_i32_f32_sdwa v32, v32 dst_sel:WORD_1 dst_unused:UNUSED_PAD src0_sel:DWORD
	v_cvt_i32_f32_e32 v33, v33
	v_lshlrev_b32_e32 v31, 8, v31
	v_and_b32_e32 v31, 0xff00, v31
	v_and_b32_e32 v32, 0xff0000, v32
	v_perm_b32 v30, v33, v30, s25
	v_or3_b32 v30, v30, v31, v32
	v_mul_f32_e32 v31, v133, v29
	global_store_dword v[20:21], v30, off offset:768
	v_mul_f32_e32 v30, v132, v29
	v_mul_f32_e32 v32, v134, v29
	v_mul_f32_e32 v33, v135, v29
	v_rndne_f32_e32 v31, v31
	v_rndne_f32_e32 v30, v30
	v_cvt_i32_f32_e32 v31, v31
	v_rndne_f32_e32 v32, v32
	v_rndne_f32_e32 v33, v33
	v_cvt_i32_f32_e32 v30, v30
	v_cvt_i32_f32_sdwa v32, v32 dst_sel:WORD_1 dst_unused:UNUSED_PAD src0_sel:DWORD
	v_cvt_i32_f32_e32 v33, v33
	v_lshlrev_b32_e32 v31, 8, v31
	v_and_b32_e32 v31, 0xff00, v31
	v_and_b32_e32 v32, 0xff0000, v32
	v_perm_b32 v30, v33, v30, s25
	v_or3_b32 v30, v30, v31, v32
	v_mul_f32_e32 v31, v137, v29
	global_store_dword v[20:21], v30, off offset:1024
	v_mul_f32_e32 v30, v136, v29
	v_mul_f32_e32 v32, v138, v29
	v_mul_f32_e32 v33, v139, v29
	v_rndne_f32_e32 v31, v31
	v_rndne_f32_e32 v30, v30
	v_cvt_i32_f32_e32 v31, v31
	v_rndne_f32_e32 v32, v32
	v_rndne_f32_e32 v33, v33
	v_cvt_i32_f32_e32 v30, v30
	v_cvt_i32_f32_sdwa v32, v32 dst_sel:WORD_1 dst_unused:UNUSED_PAD src0_sel:DWORD
	v_cvt_i32_f32_e32 v33, v33
	v_lshlrev_b32_e32 v31, 8, v31
	v_and_b32_e32 v31, 0xff00, v31
	v_and_b32_e32 v32, 0xff0000, v32
	v_perm_b32 v30, v33, v30, s25
	v_or3_b32 v30, v30, v31, v32
	v_mul_f32_e32 v31, v141, v29
	global_store_dword v[20:21], v30, off offset:1280
	v_mul_f32_e32 v30, v140, v29
	v_mul_f32_e32 v32, v142, v29
	v_mul_f32_e32 v33, v143, v29
	v_rndne_f32_e32 v31, v31
	v_rndne_f32_e32 v30, v30
	v_cvt_i32_f32_e32 v31, v31
	v_rndne_f32_e32 v32, v32
	v_rndne_f32_e32 v33, v33
	v_cvt_i32_f32_e32 v30, v30
	v_cvt_i32_f32_sdwa v32, v32 dst_sel:WORD_1 dst_unused:UNUSED_PAD src0_sel:DWORD
	v_cvt_i32_f32_e32 v33, v33
	v_lshlrev_b32_e32 v31, 8, v31
	v_and_b32_e32 v31, 0xff00, v31
	v_and_b32_e32 v32, 0xff0000, v32
	v_perm_b32 v30, v33, v30, s25
	v_or3_b32 v30, v30, v31, v32
	v_mul_f32_e32 v31, v145, v29
	global_store_dword v[20:21], v30, off offset:1536
	v_mul_f32_e32 v30, v144, v29
	v_mul_f32_e32 v32, v146, v29
	v_mul_f32_e32 v33, v147, v29
	v_rndne_f32_e32 v31, v31
	v_rndne_f32_e32 v30, v30
	v_cvt_i32_f32_e32 v31, v31
	v_rndne_f32_e32 v32, v32
	v_rndne_f32_e32 v33, v33
	v_cvt_i32_f32_e32 v30, v30
	v_cvt_i32_f32_sdwa v32, v32 dst_sel:WORD_1 dst_unused:UNUSED_PAD src0_sel:DWORD
	v_cvt_i32_f32_e32 v33, v33
	v_lshlrev_b32_e32 v31, 8, v31
	v_and_b32_e32 v31, 0xff00, v31
	v_and_b32_e32 v32, 0xff0000, v32
	v_perm_b32 v30, v33, v30, s25
	v_or3_b32 v30, v30, v31, v32
	v_mul_f32_e32 v31, v37, v29
	global_store_dword v[20:21], v30, off offset:1792
	v_mul_f32_e32 v30, v36, v29
	v_mul_f32_e32 v32, v34, v29
	v_mul_f32_e32 v33, v35, v29
	v_rndne_f32_e32 v31, v31
	v_rndne_f32_e32 v30, v30
	v_cvt_i32_f32_e32 v31, v31
	v_rndne_f32_e32 v32, v32
	v_rndne_f32_e32 v33, v33
	v_cvt_i32_f32_e32 v30, v30
	v_cvt_i32_f32_sdwa v32, v32 dst_sel:WORD_1 dst_unused:UNUSED_PAD src0_sel:DWORD
	v_cvt_i32_f32_e32 v33, v33
	v_lshlrev_b32_e32 v31, 8, v31
	v_and_b32_e32 v31, 0xff00, v31
	v_and_b32_e32 v32, 0xff0000, v32
	v_perm_b32 v30, v33, v30, s25
	v_or3_b32 v30, v30, v31, v32
	v_mul_f32_e32 v31, v151, v29
	v_mul_f32_e32 v27, v27, v29
	v_mul_f32_e32 v23, v23, v29
	v_mul_f32_e32 v17, v17, v29
	v_mul_f32_e32 v13, v13, v29
	v_mul_f32_e32 v9, v9, v29
	v_mul_f32_e32 v5, v5, v29
	global_store_dword v[20:21], v30, off offset:2048
	v_mul_f32_e32 v30, v150, v29
	v_mul_f32_e32 v32, v148, v29
	v_mul_f32_e32 v33, v149, v29
	v_rndne_f32_e32 v31, v31
	v_mul_f32_e32 v26, v26, v29
	v_mul_f32_e32 v24, v24, v29
	v_mul_f32_e32 v25, v25, v29
	v_rndne_f32_e32 v27, v27
	v_mul_f32_e32 v22, v22, v29
	v_mul_f32_e32 v18, v18, v29
	v_mul_f32_e32 v19, v19, v29
	v_rndne_f32_e32 v23, v23
	v_mul_f32_e32 v16, v16, v29
	v_mul_f32_e32 v14, v14, v29
	v_mul_f32_e32 v15, v15, v29
	v_rndne_f32_e32 v17, v17
	v_mul_f32_e32 v12, v12, v29
	v_mul_f32_e32 v10, v10, v29
	v_mul_f32_e32 v11, v11, v29
	v_rndne_f32_e32 v13, v13
	v_mul_f32_e32 v8, v8, v29
	v_mul_f32_e32 v6, v6, v29
	v_mul_f32_e32 v7, v7, v29
	v_rndne_f32_e32 v9, v9
	v_mul_f32_e32 v4, v4, v29
	v_mul_f32_e32 v2, v2, v29
	v_mul_f32_e32 v3, v3, v29
	v_rndne_f32_e32 v5, v5
	v_rndne_f32_e32 v30, v30
	v_cvt_i32_f32_e32 v31, v31
	v_rndne_f32_e32 v32, v32
	v_rndne_f32_e32 v33, v33
	v_rndne_f32_e32 v26, v26
	v_cvt_i32_f32_e32 v27, v27
	v_rndne_f32_e32 v24, v24
	v_rndne_f32_e32 v25, v25
	v_rndne_f32_e32 v22, v22
	v_cvt_i32_f32_e32 v23, v23
	v_rndne_f32_e32 v18, v18
	v_rndne_f32_e32 v19, v19
	v_rndne_f32_e32 v16, v16
	v_cvt_i32_f32_e32 v17, v17
	v_rndne_f32_e32 v14, v14
	v_rndne_f32_e32 v15, v15
	v_rndne_f32_e32 v12, v12
	v_cvt_i32_f32_e32 v13, v13
	v_rndne_f32_e32 v10, v10
	v_rndne_f32_e32 v11, v11
	v_rndne_f32_e32 v8, v8
	v_cvt_i32_f32_e32 v9, v9
	v_rndne_f32_e32 v6, v6
	v_rndne_f32_e32 v7, v7
	v_rndne_f32_e32 v4, v4
	v_cvt_i32_f32_e32 v5, v5
	v_rndne_f32_e32 v2, v2
	v_rndne_f32_e32 v3, v3
	v_cvt_i32_f32_e32 v30, v30
	v_cvt_i32_f32_sdwa v32, v32 dst_sel:WORD_1 dst_unused:UNUSED_PAD src0_sel:DWORD
	v_cvt_i32_f32_e32 v33, v33
	v_cvt_i32_f32_e32 v26, v26
	v_cvt_i32_f32_sdwa v24, v24 dst_sel:WORD_1 dst_unused:UNUSED_PAD src0_sel:DWORD
	v_cvt_i32_f32_e32 v25, v25
	v_cvt_i32_f32_e32 v22, v22
	v_cvt_i32_f32_sdwa v18, v18 dst_sel:WORD_1 dst_unused:UNUSED_PAD src0_sel:DWORD
	v_cvt_i32_f32_e32 v19, v19
	v_cvt_i32_f32_e32 v16, v16
	v_cvt_i32_f32_sdwa v14, v14 dst_sel:WORD_1 dst_unused:UNUSED_PAD src0_sel:DWORD
	v_cvt_i32_f32_e32 v15, v15
	v_cvt_i32_f32_e32 v12, v12
	v_cvt_i32_f32_sdwa v10, v10 dst_sel:WORD_1 dst_unused:UNUSED_PAD src0_sel:DWORD
	v_cvt_i32_f32_e32 v11, v11
	v_cvt_i32_f32_e32 v8, v8
	v_cvt_i32_f32_sdwa v6, v6 dst_sel:WORD_1 dst_unused:UNUSED_PAD src0_sel:DWORD
	v_cvt_i32_f32_e32 v7, v7
	v_cvt_i32_f32_e32 v4, v4
	v_cvt_i32_f32_sdwa v2, v2 dst_sel:WORD_1 dst_unused:UNUSED_PAD src0_sel:DWORD
	v_cvt_i32_f32_e32 v3, v3
	v_lshlrev_b32_e32 v31, 8, v31
	v_lshlrev_b32_e32 v27, 8, v27
	v_lshlrev_b32_e32 v23, 8, v23
	v_lshlrev_b32_e32 v17, 8, v17
	v_lshlrev_b32_e32 v13, 8, v13
	v_lshlrev_b32_e32 v9, 8, v9
	v_lshlrev_b32_e32 v5, 8, v5
	v_and_b32_e32 v31, 0xff00, v31
	v_and_b32_e32 v32, 0xff0000, v32
	v_perm_b32 v30, v33, v30, s25
	v_and_b32_e32 v27, 0xff00, v27
	v_and_b32_e32 v24, 0xff0000, v24
	v_perm_b32 v25, v25, v26, s25
	v_and_b32_e32 v23, 0xff00, v23
	v_and_b32_e32 v18, 0xff0000, v18
	v_perm_b32 v19, v19, v22, s25
	v_and_b32_e32 v17, 0xff00, v17
	v_and_b32_e32 v14, 0xff0000, v14
	v_perm_b32 v15, v15, v16, s25
	v_and_b32_e32 v13, 0xff00, v13
	v_and_b32_e32 v10, 0xff0000, v10
	v_perm_b32 v11, v11, v12, s25
	v_and_b32_e32 v9, 0xff00, v9
	v_and_b32_e32 v6, 0xff0000, v6
	v_perm_b32 v7, v7, v8, s25
	v_and_b32_e32 v5, 0xff00, v5
	v_and_b32_e32 v2, 0xff0000, v2
	v_perm_b32 v3, v3, v4, s25
	v_or3_b32 v30, v30, v31, v32
	v_or3_b32 v24, v25, v27, v24
	v_or3_b32 v18, v19, v23, v18
	v_or3_b32 v14, v15, v17, v14
	v_or3_b32 v10, v11, v13, v10
	v_or3_b32 v6, v7, v9, v6
	v_or3_b32 v2, v3, v5, v2
	global_store_dword v[20:21], v30, off offset:2304
	global_store_dword v[20:21], v24, off offset:2560
	global_store_dword v[20:21], v18, off offset:2816
	global_store_dword v[20:21], v14, off offset:3072
	global_store_dword v[20:21], v10, off offset:3328
	global_store_dword v[20:21], v6, off offset:3584
	global_store_dword v[20:21], v2, off offset:3840
	s_and_saveexec_b64 s[8:9], s[6:7]
	s_cbranch_execz .LBB0_92
	s_add_u32 s28, s4, s16
	s_addc_u32 s29, s5, s17
	v_mul_f32_e32 v2, 0x3c010204, v28
	global_store_dword v69, v2, s[28:29]
	s_branch .LBB0_92
